# P4b merge epilogue: running sum Mg of row groups 0-2 kept in registers across the 3 branch units (no store for br<2, no sc1 reload for br>0); merge Y prefetch dropped to free the registers
# speedup vs baseline: 1.0286x; 1.0037x over previous
.LBB0_802:
	s_cmp_gt_u32 s0, 7
	s_cselect_b64 s[34:35], -1, 0
	s_lshl_b32 s1, s0, 8
	s_and_b32 s26, s1, 0xfffffc00
	s_ashr_i32 s27, s26, 31
	s_and_b32 s19, s1, 0x300
	s_lshl_b64 s[30:31], s[26:27], 2
	v_or_b32_e32 v0, s19, v191
	s_add_u32 s30, s56, s30
	v_lshl_add_u32 v162, s28, 8, v190
	v_mov_b64_e32 v[18:19], s[12:13]
	s_movk_i32 s66, 0x1800
	s_addc_u32 s31, s57, s31
	v_lshlrev_b32_e32 v6, 2, v0
	v_mad_i64_i32 v[18:19], s[28:29], v162, s66, v[18:19]
	s_nop 15
	s_nop 3
	global_load_dwordx4 v[10:13], v6, s[30:31] offset:16
	global_load_dwordx4 v[14:17], v6, s[30:31]
	global_load_dwordx4 v[2:5], v6, s[30:31] offset:528
	s_nop 0
	global_load_dwordx4 v[6:9], v6, s[30:31] offset:512
	v_lshl_add_u64 v[18:19], s[26:27], 1, v[18:19]
	v_lshlrev_b32_e32 v0, 1, v0
	v_lshl_add_u64 v[18:19], v[18:19], 0, v[0:1]
	global_load_dwordx4 v[30:33], v[18:19], off
	v_ashrrev_i32_e32 v163, 31, v162
	s_cmp_gt_u32 s0, 3
	s_cselect_b64 s[28:29], -1, 0
	v_lshlrev_b64 v[20:21], 11, v[162:163]
	v_readlane_b32 s68, v253, 41
	v_lshl_add_u64 v[178:179], s[10:11], 0, v[20:21]
	v_mov_b32_e32 v176, 0
	s_and_b64 vcc, exec, s[28:29]
	v_mov_b32_e32 v182, 0
	v_mov_b32_e32 v183, 0
	v_mov_b32_e32 v180, 0
	v_mov_b32_e32 v181, 0
	v_readlane_b32 s69, v253, 42
	v_readlane_b32 s67, v253, 52
	s_cbranch_vccz .LBB0_804
	v_lshl_add_u64 v[20:21], v[178:179], 0, v[0:1]
	v_mov_b32_e32 v182, v224
	v_mov_b32_e32 v183, v225
	v_mov_b32_e32 v180, v226
	v_mov_b32_e32 v181, v227
.LBB0_804:
	global_load_dwordx4 v[22:25], v[18:19], off offset:256
	v_cndmask_b32_e64 v18, 0, 1, s[28:29]
	v_cmp_ne_u32_e64 s[0:1], 1, v18
	s_andn2_b64 vcc, exec, s[28:29]
	v_mov_b32_e32 v177, 0
	v_mov_b32_e32 v174, 0
	v_mov_b32_e32 v175, 0
	s_cbranch_vccnz .LBB0_806
	v_lshl_add_u64 v[18:19], v[178:179], 0, v[0:1]
	v_mov_b32_e32 v176, v228
	v_mov_b32_e32 v177, v229
	v_mov_b32_e32 v174, v230
	v_mov_b32_e32 v175, v231
.LBB0_806:
	v_or_b32_e32 v20, 16, v162
	v_mov_b64_e32 v[18:19], s[12:13]
	v_mad_i64_i32 v[18:19], s[28:29], v20, s66, v[18:19]
	v_lshl_add_u64 v[18:19], s[26:27], 1, v[18:19]
	v_lshl_add_u64 v[18:19], v[18:19], 0, v[0:1]
	global_load_dwordx4 v[26:29], v[18:19], off
	v_ashrrev_i32_e32 v21, 31, v20
	v_lshlrev_b64 v[20:21], 11, v[20:21]
	v_lshl_add_u64 v[168:169], s[10:11], 0, v[20:21]
	v_mov_b32_e32 v166, 0
	s_and_b64 vcc, exec, s[0:1]
	v_mov_b32_e32 v172, 0
	v_mov_b32_e32 v173, 0
	v_mov_b32_e32 v170, 0
	v_mov_b32_e32 v171, 0
	s_mov_b32 s70, 0xe000
	s_cbranch_vccnz .LBB0_808
	v_lshl_add_u64 v[20:21], v[168:169], 0, v[0:1]
	v_mov_b32_e32 v172, v232
	v_mov_b32_e32 v173, v233
	v_mov_b32_e32 v170, v234
	v_mov_b32_e32 v171, v235
.LBB0_808:
	s_nop 0
	global_load_dwordx4 v[18:21], v[18:19], off offset:256
	s_and_b64 vcc, exec, s[0:1]
	v_mov_b32_e32 v167, 0
	v_mov_b32_e32 v164, 0
	v_mov_b32_e32 v165, 0
	s_cbranch_vccnz .LBB0_810
	v_lshl_add_u64 v[164:165], v[168:169], 0, v[0:1]
	v_mov_b32_e32 v166, v236
	v_mov_b32_e32 v167, v237
	s_nop 0
	v_mov_b32_e32 v164, v238
	v_mov_b32_e32 v165, v239
.LBB0_810:
	s_waitcnt vmcnt(6)
	v_add_f32_e32 v158, v158, v14
	v_add_f32_e32 v159, v159, v15
	v_mul_f32_e32 v158, 0xbfb8aa3b, v158
	v_mul_f32_e32 v159, 0xbfb8aa3b, v159
	v_exp_f32_e32 v158, v158
	v_exp_f32_e32 v159, v159
	s_waitcnt vmcnt(3)
	v_lshlrev_b32_e32 v194, 16, v30
	v_and_b32_e32 v195, 0xffff0000, v30
	v_add_f32_e32 v30, v160, v16
	v_mul_f32_e32 v30, 0xbfb8aa3b, v30
	v_add_f32_e32 v160, v161, v17
	v_exp_f32_e32 v30, v30
	v_mul_f32_e32 v160, 0xbfb8aa3b, v160
	v_exp_f32_e32 v161, v160
	v_add_f32_e32 v158, 1.0, v158
	v_add_f32_e32 v159, 1.0, v159
	v_rcp_f32_e32 v158, v158
	v_rcp_f32_e32 v159, v159
	v_add_f32_e32 v154, v154, v10
	v_add_f32_e32 v30, 1.0, v30
	v_mul_f32_e32 v154, 0xbfb8aa3b, v154
	v_rcp_f32_e32 v160, v30
	v_add_f32_e32 v30, 1.0, v161
	v_exp_f32_e32 v163, v154
	v_add_f32_e32 v154, v155, v11
	v_lshlrev_b32_e32 v196, 16, v182
	v_and_b32_e32 v197, 0xffff0000, v182
	v_rcp_f32_e32 v161, v30
	v_mul_f32_e32 v154, 0xbfb8aa3b, v154
	v_pk_fma_f32 v[158:159], v[158:159], v[194:195], v[196:197]
	v_exp_f32_e32 v194, v154
	v_lshlrev_b32_e32 v30, 16, v31
	v_and_b32_e32 v31, 0xffff0000, v31
	v_lshlrev_b32_e32 v182, 16, v183
	v_and_b32_e32 v183, 0xffff0000, v183
	v_pk_fma_f32 v[154:155], v[160:161], v[30:31], v[182:183]
	v_lshlrev_b32_e32 v160, 16, v32
	v_and_b32_e32 v161, 0xffff0000, v32
	v_add_f32_e32 v32, v156, v12
	v_add_f32_e32 v156, v157, v13
	v_add_f32_e32 v30, 1.0, v163
	v_add_f32_e32 v31, 1.0, v194
	v_mul_f32_e32 v32, 0xbfb8aa3b, v32
	v_mul_f32_e32 v156, 0xbfb8aa3b, v156
	v_rcp_f32_e32 v30, v30
	v_rcp_f32_e32 v31, v31
	v_exp_f32_e32 v32, v32
	v_exp_f32_e32 v163, v156
	v_lshlrev_b32_e32 v182, 16, v180
	v_and_b32_e32 v183, 0xffff0000, v180
	v_pk_fma_f32 v[156:157], v[30:31], v[160:161], v[182:183]
	v_add_f32_e32 v30, 1.0, v32
	v_add_f32_e32 v31, 1.0, v163
	v_rcp_f32_e32 v30, v30
	v_rcp_f32_e32 v31, v31
	v_add_f32_e32 v150, v150, v6
	v_add_f32_e32 v151, v151, v7
	v_lshlrev_b32_e32 v32, 16, v33
	v_and_b32_e32 v33, 0xffff0000, v33
	v_lshlrev_b32_e32 v160, 16, v181
	v_and_b32_e32 v161, 0xffff0000, v181
	v_mul_f32_e32 v150, 0xbfb8aa3b, v150
	v_mul_f32_e32 v151, 0xbfb8aa3b, v151
	v_pk_fma_f32 v[160:161], v[30:31], v[32:33], v[160:161]
	v_exp_f32_e32 v150, v150
	v_exp_f32_e32 v151, v151
	v_cvt_pk_bf16_f32 v30, v158, v159
	v_cvt_pk_bf16_f32 v31, v154, v155
	v_cvt_pk_bf16_f32 v32, v156, v157
	v_cvt_pk_bf16_f32 v33, v160, v161
	v_lshl_add_u64 v[154:155], v[178:179], 0, v[0:1]
	v_mov_b32_e32 v224, v30
	v_mov_b32_e32 v225, v31
	v_mov_b32_e32 v226, v32
	v_mov_b32_e32 v227, v33
	s_mov_b64 exec, s[34:35]
	global_store_dwordx4 v[154:155], v[30:33], off
	s_mov_b64 exec, -1
	v_add_f32_e32 v146, v146, v2
	v_add_f32_e32 v147, v147, v3
	s_waitcnt vmcnt(3)
	v_lshlrev_b32_e32 v32, 16, v22
	v_and_b32_e32 v33, 0xffff0000, v22
	v_add_f32_e32 v22, v152, v8
	v_mul_f32_e32 v22, 0xbfb8aa3b, v22
	v_add_f32_e32 v152, v153, v9
	v_add_f32_e32 v30, 1.0, v150
	v_add_f32_e32 v31, 1.0, v151
	v_exp_f32_e32 v22, v22
	v_mul_f32_e32 v152, 0xbfb8aa3b, v152
	v_rcp_f32_e32 v30, v30
	v_rcp_f32_e32 v31, v31
	v_exp_f32_e32 v152, v152
	v_lshlrev_b32_e32 v150, 16, v176
	v_and_b32_e32 v151, 0xffff0000, v176
	v_add_f32_e32 v22, 1.0, v22
	v_pk_fma_f32 v[30:31], v[30:31], v[32:33], v[150:151]
	v_rcp_f32_e32 v32, v22
	v_add_f32_e32 v22, 1.0, v152
	v_mul_f32_e32 v146, 0xbfb8aa3b, v146
	v_mul_f32_e32 v147, 0xbfb8aa3b, v147
	v_rcp_f32_e32 v33, v22
	v_exp_f32_e32 v146, v146
	v_exp_f32_e32 v147, v147
	v_lshlrev_b32_e32 v22, 16, v23
	v_and_b32_e32 v23, 0xffff0000, v23
	v_lshlrev_b32_e32 v150, 16, v177
	v_and_b32_e32 v151, 0xffff0000, v177
	v_pk_fma_f32 v[32:33], v[32:33], v[22:23], v[150:151]
	v_add_f32_e32 v22, 1.0, v146
	v_add_f32_e32 v23, 1.0, v147
	v_lshlrev_b32_e32 v146, 16, v24
	v_and_b32_e32 v147, 0xffff0000, v24
	v_add_f32_e32 v24, v148, v4
	v_add_f32_e32 v148, v149, v5
	v_mul_f32_e32 v24, 0xbfb8aa3b, v24
	v_mul_f32_e32 v148, 0xbfb8aa3b, v148
	v_rcp_f32_e32 v22, v22
	v_rcp_f32_e32 v23, v23
	v_exp_f32_e32 v24, v24
	v_exp_f32_e32 v148, v148
	v_lshlrev_b32_e32 v150, 16, v174
	v_and_b32_e32 v151, 0xffff0000, v174
	v_pk_fma_f32 v[146:147], v[22:23], v[146:147], v[150:151]
	v_add_f32_e32 v22, 1.0, v24
	v_add_f32_e32 v23, 1.0, v148
	v_rcp_f32_e32 v22, v22
	v_rcp_f32_e32 v23, v23
	v_lshlrev_b32_e32 v24, 16, v25
	v_and_b32_e32 v25, 0xffff0000, v25
	v_lshlrev_b32_e32 v148, 16, v175
	v_and_b32_e32 v149, 0xffff0000, v175
	v_pk_fma_f32 v[148:149], v[22:23], v[24:25], v[148:149]
	v_cvt_pk_bf16_f32 v22, v30, v31
	v_cvt_pk_bf16_f32 v23, v32, v33
	v_cvt_pk_bf16_f32 v24, v146, v147
	v_cvt_pk_bf16_f32 v25, v148, v149
	v_mov_b32_e32 v228, v22
	v_mov_b32_e32 v229, v23
	v_mov_b32_e32 v230, v24
	v_mov_b32_e32 v231, v25
	s_mov_b64 exec, s[34:35]
	global_store_dwordx4 v[154:155], v[22:25], off offset:256
	s_mov_b64 exec, -1
	v_mov_b32_e32 v148, 0
	s_and_b64 vcc, exec, s[0:1]
	v_or_b32_e32 v24, 32, v162
	v_mov_b64_e32 v[22:23], s[12:13]
	v_mad_i64_i32 v[22:23], s[28:29], v24, s66, v[22:23]
	v_lshl_add_u64 v[22:23], s[26:27], 1, v[22:23]
	v_lshl_add_u64 v[22:23], v[22:23], 0, v[0:1]
	global_load_dwordx4 v[30:33], v[22:23], off
	v_ashrrev_i32_e32 v25, 31, v24
	v_lshlrev_b64 v[24:25], 11, v[24:25]
	v_lshl_add_u64 v[150:151], s[10:11], 0, v[24:25]
	v_mov_b32_e32 v154, 0
	v_mov_b32_e32 v155, 0
	v_mov_b32_e32 v152, 0
	v_mov_b32_e32 v153, 0
	s_cbranch_vccnz .LBB0_812
	v_lshl_add_u64 v[24:25], v[150:151], 0, v[0:1]
	v_mov_b32_e32 v154, v240
	v_mov_b32_e32 v155, v241
	v_mov_b32_e32 v152, v246
	v_mov_b32_e32 v153, v247
.LBB0_812:
	s_nop 0
	global_load_dwordx4 v[22:25], v[22:23], off offset:256
	s_and_b64 vcc, exec, s[0:1]
	v_mov_b32_e32 v149, 0
	v_mov_b32_e32 v146, 0
	v_mov_b32_e32 v147, 0
	s_cbranch_vccnz .LBB0_814
	v_lshl_add_u64 v[146:147], v[150:151], 0, v[0:1]
	v_mov_b32_e32 v148, v216
	v_mov_b32_e32 v149, v217
	s_nop 0
	v_mov_b32_e32 v146, v218
	v_mov_b32_e32 v147, v219
.LBB0_814:
	v_add_f32_e32 v142, v142, v14
	v_add_f32_e32 v143, v143, v15
	v_mul_f32_e32 v142, 0xbfb8aa3b, v142
	v_mul_f32_e32 v143, 0xbfb8aa3b, v143
	v_exp_f32_e32 v142, v142
	v_exp_f32_e32 v143, v143
	s_waitcnt vmcnt(5)
	v_lshlrev_b32_e32 v156, 16, v26
	v_and_b32_e32 v157, 0xffff0000, v26
	v_add_f32_e32 v26, v144, v16
	v_mul_f32_e32 v26, 0xbfb8aa3b, v26
	v_add_f32_e32 v144, v145, v17
	v_add_f32_e32 v142, 1.0, v142
	v_add_f32_e32 v143, 1.0, v143
	v_exp_f32_e32 v26, v26
	v_mul_f32_e32 v144, 0xbfb8aa3b, v144
	v_rcp_f32_e32 v142, v142
	v_rcp_f32_e32 v143, v143
	v_exp_f32_e32 v145, v144
	v_add_f32_e32 v138, v138, v10
	v_lshlrev_b32_e32 v158, 16, v172
	v_and_b32_e32 v159, 0xffff0000, v172
	v_add_f32_e32 v26, 1.0, v26
	v_mul_f32_e32 v138, 0xbfb8aa3b, v138
	v_pk_fma_f32 v[142:143], v[142:143], v[156:157], v[158:159]
	v_rcp_f32_e32 v144, v26
	v_add_f32_e32 v26, 1.0, v145
	v_exp_f32_e32 v158, v138
	v_add_f32_e32 v138, v139, v11
	v_rcp_f32_e32 v145, v26
	v_mul_f32_e32 v138, 0xbfb8aa3b, v138
	v_exp_f32_e32 v159, v138
	v_lshlrev_b32_e32 v26, 16, v27
	v_and_b32_e32 v27, 0xffff0000, v27
	v_lshlrev_b32_e32 v156, 16, v173
	v_and_b32_e32 v157, 0xffff0000, v173
	v_pk_fma_f32 v[138:139], v[144:145], v[26:27], v[156:157]
	v_lshlrev_b32_e32 v144, 16, v28
	v_and_b32_e32 v145, 0xffff0000, v28
	v_add_f32_e32 v28, v140, v12
	v_add_f32_e32 v140, v141, v13
	v_add_f32_e32 v26, 1.0, v158
	v_add_f32_e32 v27, 1.0, v159
	v_mul_f32_e32 v28, 0xbfb8aa3b, v28
	v_mul_f32_e32 v140, 0xbfb8aa3b, v140
	v_rcp_f32_e32 v26, v26
	v_rcp_f32_e32 v27, v27
	v_exp_f32_e32 v28, v28
	v_exp_f32_e32 v158, v140
	v_lshlrev_b32_e32 v156, 16, v170
	v_and_b32_e32 v157, 0xffff0000, v170
	v_pk_fma_f32 v[140:141], v[26:27], v[144:145], v[156:157]
	v_add_f32_e32 v26, 1.0, v28
	v_add_f32_e32 v27, 1.0, v158
	v_rcp_f32_e32 v26, v26
	v_rcp_f32_e32 v27, v27
	v_add_f32_e32 v134, v134, v6
	v_add_f32_e32 v135, v135, v7
	v_lshlrev_b32_e32 v28, 16, v29
	v_and_b32_e32 v29, 0xffff0000, v29
	v_lshlrev_b32_e32 v144, 16, v171
	v_and_b32_e32 v145, 0xffff0000, v171
	v_mul_f32_e32 v134, 0xbfb8aa3b, v134
	v_mul_f32_e32 v135, 0xbfb8aa3b, v135
	v_pk_fma_f32 v[144:145], v[26:27], v[28:29], v[144:145]
	v_exp_f32_e32 v134, v134
	v_exp_f32_e32 v135, v135
	v_cvt_pk_bf16_f32 v26, v142, v143
	v_cvt_pk_bf16_f32 v27, v138, v139
	v_cvt_pk_bf16_f32 v28, v140, v141
	v_cvt_pk_bf16_f32 v29, v144, v145
	v_lshl_add_u64 v[138:139], v[168:169], 0, v[0:1]
	v_mov_b32_e32 v232, v26
	v_mov_b32_e32 v233, v27
	v_mov_b32_e32 v234, v28
	v_mov_b32_e32 v235, v29
	s_mov_b64 exec, s[34:35]
	global_store_dwordx4 v[138:139], v[26:29], off
	s_mov_b64 exec, -1
	v_add_f32_e32 v130, v130, v2
	v_add_f32_e32 v131, v131, v3
	s_waitcnt vmcnt(5)
	v_lshlrev_b32_e32 v28, 16, v18
	v_and_b32_e32 v29, 0xffff0000, v18
	v_add_f32_e32 v18, v136, v8
	v_mul_f32_e32 v18, 0xbfb8aa3b, v18
	v_add_f32_e32 v136, v137, v9
	v_add_f32_e32 v26, 1.0, v134
	v_add_f32_e32 v27, 1.0, v135
	v_exp_f32_e32 v18, v18
	v_mul_f32_e32 v136, 0xbfb8aa3b, v136
	v_rcp_f32_e32 v26, v26
	v_rcp_f32_e32 v27, v27
	v_exp_f32_e32 v136, v136
	v_lshlrev_b32_e32 v134, 16, v166
	v_and_b32_e32 v135, 0xffff0000, v166
	v_add_f32_e32 v18, 1.0, v18
	v_pk_fma_f32 v[26:27], v[26:27], v[28:29], v[134:135]
	v_rcp_f32_e32 v28, v18
	v_add_f32_e32 v18, 1.0, v136
	v_mul_f32_e32 v130, 0xbfb8aa3b, v130
	v_mul_f32_e32 v131, 0xbfb8aa3b, v131
	v_rcp_f32_e32 v29, v18
	v_exp_f32_e32 v130, v130
	v_exp_f32_e32 v131, v131
	v_lshlrev_b32_e32 v18, 16, v19
	v_and_b32_e32 v19, 0xffff0000, v19
	v_lshlrev_b32_e32 v134, 16, v167
	v_and_b32_e32 v135, 0xffff0000, v167
	v_pk_fma_f32 v[28:29], v[28:29], v[18:19], v[134:135]
	v_add_f32_e32 v18, 1.0, v130
	v_add_f32_e32 v19, 1.0, v131
	v_lshlrev_b32_e32 v130, 16, v20
	v_and_b32_e32 v131, 0xffff0000, v20
	v_add_f32_e32 v20, v132, v4
	v_add_f32_e32 v132, v133, v5
	v_mul_f32_e32 v20, 0xbfb8aa3b, v20
	v_mul_f32_e32 v132, 0xbfb8aa3b, v132
	v_rcp_f32_e32 v18, v18
	v_rcp_f32_e32 v19, v19
	v_exp_f32_e32 v20, v20
	v_exp_f32_e32 v132, v132
	v_lshlrev_b32_e32 v134, 16, v164
	v_and_b32_e32 v135, 0xffff0000, v164
	v_pk_fma_f32 v[130:131], v[18:19], v[130:131], v[134:135]
	v_add_f32_e32 v18, 1.0, v20
	v_add_f32_e32 v19, 1.0, v132
	v_rcp_f32_e32 v18, v18
	v_rcp_f32_e32 v19, v19
	v_lshlrev_b32_e32 v20, 16, v21
	v_and_b32_e32 v21, 0xffff0000, v21
	v_lshlrev_b32_e32 v132, 16, v165
	v_and_b32_e32 v133, 0xffff0000, v165
	v_pk_fma_f32 v[132:133], v[18:19], v[20:21], v[132:133]
	v_cvt_pk_bf16_f32 v18, v26, v27
	v_cvt_pk_bf16_f32 v19, v28, v29
	v_cvt_pk_bf16_f32 v20, v130, v131
	v_cvt_pk_bf16_f32 v21, v132, v133
	v_mov_b32_e32 v236, v18
	v_mov_b32_e32 v237, v19
	v_mov_b32_e32 v238, v20
	v_mov_b32_e32 v239, v21
	s_mov_b64 exec, s[34:35]
	global_store_dwordx4 v[138:139], v[18:21], off offset:256
	s_mov_b64 exec, -1
	v_mov_b32_e32 v132, 0
	s_and_b64 vcc, exec, s[0:1]
	v_or_b32_e32 v20, 48, v162
	v_mov_b64_e32 v[18:19], s[12:13]
	v_mad_i64_i32 v[18:19], s[28:29], v20, s66, v[18:19]
	v_lshl_add_u64 v[18:19], s[26:27], 1, v[18:19]
	v_lshl_add_u64 v[18:19], v[18:19], 0, v[0:1]
	global_load_dwordx4 v[26:29], v[18:19], off
	v_ashrrev_i32_e32 v21, 31, v20
	v_lshlrev_b64 v[20:21], 11, v[20:21]
	v_lshl_add_u64 v[134:135], s[10:11], 0, v[20:21]
	v_mov_b32_e32 v138, 0
	v_mov_b32_e32 v139, 0
	v_mov_b32_e32 v136, 0
	v_mov_b32_e32 v137, 0
	s_cbranch_vccnz .LBB0_816
	v_lshl_add_u64 v[20:21], v[134:135], 0, v[0:1]
	global_load_dwordx2 v[138:139], v[20:21], off sc1
	global_load_dwordx2 v[136:137], v[20:21], off offset:8 sc1

.LBB0_818:
	v_add_f32_e32 v126, v126, v14
	v_add_f32_e32 v127, v127, v15
	v_mul_f32_e32 v126, 0xbfb8aa3b, v126
	v_mul_f32_e32 v127, 0xbfb8aa3b, v127
	v_exp_f32_e32 v126, v126
	v_exp_f32_e32 v127, v127
	s_waitcnt vmcnt(5)
	v_lshlrev_b32_e32 v140, 16, v30
	v_and_b32_e32 v141, 0xffff0000, v30
	v_add_f32_e32 v30, v128, v16
	v_mul_f32_e32 v30, 0xbfb8aa3b, v30
	v_add_f32_e32 v128, v129, v17
	v_add_f32_e32 v126, 1.0, v126
	v_add_f32_e32 v127, 1.0, v127
	v_exp_f32_e32 v30, v30
	v_mul_f32_e32 v128, 0xbfb8aa3b, v128
	v_rcp_f32_e32 v126, v126
	v_rcp_f32_e32 v127, v127
	v_exp_f32_e32 v129, v128
	v_add_f32_e32 v122, v122, v10
	v_lshlrev_b32_e32 v142, 16, v154
	v_and_b32_e32 v143, 0xffff0000, v154
	v_add_f32_e32 v30, 1.0, v30
	v_mul_f32_e32 v122, 0xbfb8aa3b, v122
	v_pk_fma_f32 v[126:127], v[126:127], v[140:141], v[142:143]
	v_rcp_f32_e32 v128, v30
	v_add_f32_e32 v30, 1.0, v129
	v_exp_f32_e32 v142, v122
	v_add_f32_e32 v122, v123, v11
	v_rcp_f32_e32 v129, v30
	v_mul_f32_e32 v122, 0xbfb8aa3b, v122
	v_exp_f32_e32 v143, v122
	v_lshlrev_b32_e32 v30, 16, v31
	v_and_b32_e32 v31, 0xffff0000, v31
	v_lshlrev_b32_e32 v140, 16, v155
	v_and_b32_e32 v141, 0xffff0000, v155
	v_pk_fma_f32 v[122:123], v[128:129], v[30:31], v[140:141]
	v_lshlrev_b32_e32 v128, 16, v32
	v_and_b32_e32 v129, 0xffff0000, v32
	v_add_f32_e32 v32, v124, v12
	v_add_f32_e32 v124, v125, v13
	v_add_f32_e32 v30, 1.0, v142
	v_add_f32_e32 v31, 1.0, v143
	v_mul_f32_e32 v32, 0xbfb8aa3b, v32
	v_mul_f32_e32 v124, 0xbfb8aa3b, v124
	v_rcp_f32_e32 v30, v30
	v_rcp_f32_e32 v31, v31
	v_exp_f32_e32 v32, v32
	v_exp_f32_e32 v142, v124
	v_lshlrev_b32_e32 v140, 16, v152
	v_and_b32_e32 v141, 0xffff0000, v152
	v_pk_fma_f32 v[124:125], v[30:31], v[128:129], v[140:141]
	v_add_f32_e32 v30, 1.0, v32
	v_add_f32_e32 v31, 1.0, v142
	v_rcp_f32_e32 v30, v30
	v_rcp_f32_e32 v31, v31
	v_add_f32_e32 v118, v118, v6
	v_add_f32_e32 v119, v119, v7
	v_lshlrev_b32_e32 v32, 16, v33
	v_and_b32_e32 v33, 0xffff0000, v33
	v_lshlrev_b32_e32 v128, 16, v153
	v_and_b32_e32 v129, 0xffff0000, v153
	v_mul_f32_e32 v118, 0xbfb8aa3b, v118
	v_mul_f32_e32 v119, 0xbfb8aa3b, v119
	v_pk_fma_f32 v[128:129], v[30:31], v[32:33], v[128:129]
	v_exp_f32_e32 v118, v118
	v_exp_f32_e32 v119, v119
	v_cvt_pk_bf16_f32 v30, v126, v127
	v_cvt_pk_bf16_f32 v31, v122, v123
	v_cvt_pk_bf16_f32 v32, v124, v125
	v_cvt_pk_bf16_f32 v33, v128, v129
	v_lshl_add_u64 v[122:123], v[150:151], 0, v[0:1]
	v_mov_b32_e32 v240, v30
	v_mov_b32_e32 v241, v31
	v_mov_b32_e32 v246, v32
	v_mov_b32_e32 v247, v33
	s_mov_b64 exec, s[34:35]
	global_store_dwordx4 v[122:123], v[30:33], off
	s_mov_b64 exec, -1
	v_add_f32_e32 v114, v114, v2
	v_add_f32_e32 v115, v115, v3
	s_waitcnt vmcnt(5)
	v_lshlrev_b32_e32 v32, 16, v22
	v_and_b32_e32 v33, 0xffff0000, v22
	v_add_f32_e32 v22, v120, v8
	v_mul_f32_e32 v22, 0xbfb8aa3b, v22
	v_add_f32_e32 v120, v121, v9
	v_add_f32_e32 v30, 1.0, v118
	v_add_f32_e32 v31, 1.0, v119
	v_exp_f32_e32 v22, v22
	v_mul_f32_e32 v120, 0xbfb8aa3b, v120
	v_rcp_f32_e32 v30, v30
	v_rcp_f32_e32 v31, v31
	v_exp_f32_e32 v120, v120
	v_lshlrev_b32_e32 v118, 16, v148
	v_and_b32_e32 v119, 0xffff0000, v148
	v_add_f32_e32 v22, 1.0, v22
	v_pk_fma_f32 v[30:31], v[30:31], v[32:33], v[118:119]
	v_rcp_f32_e32 v32, v22
	v_add_f32_e32 v22, 1.0, v120
	v_mul_f32_e32 v114, 0xbfb8aa3b, v114
	v_mul_f32_e32 v115, 0xbfb8aa3b, v115
	v_rcp_f32_e32 v33, v22
	v_exp_f32_e32 v114, v114
	v_exp_f32_e32 v115, v115
	v_lshlrev_b32_e32 v22, 16, v23
	v_and_b32_e32 v23, 0xffff0000, v23
	v_lshlrev_b32_e32 v118, 16, v149
	v_and_b32_e32 v119, 0xffff0000, v149
	v_pk_fma_f32 v[32:33], v[32:33], v[22:23], v[118:119]
	v_add_f32_e32 v22, 1.0, v114
	v_add_f32_e32 v23, 1.0, v115
	v_lshlrev_b32_e32 v114, 16, v24
	v_and_b32_e32 v115, 0xffff0000, v24
	v_add_f32_e32 v24, v116, v4
	v_add_f32_e32 v116, v117, v5
	v_mul_f32_e32 v24, 0xbfb8aa3b, v24
	v_mul_f32_e32 v116, 0xbfb8aa3b, v116
	v_rcp_f32_e32 v22, v22
	v_rcp_f32_e32 v23, v23
	v_exp_f32_e32 v24, v24
	v_exp_f32_e32 v116, v116
	v_lshlrev_b32_e32 v118, 16, v146
	v_and_b32_e32 v119, 0xffff0000, v146
	v_pk_fma_f32 v[114:115], v[22:23], v[114:115], v[118:119]
	v_add_f32_e32 v22, 1.0, v24
	v_add_f32_e32 v23, 1.0, v116
	v_rcp_f32_e32 v22, v22
	v_rcp_f32_e32 v23, v23
	v_lshlrev_b32_e32 v24, 16, v25
	v_and_b32_e32 v25, 0xffff0000, v25
	v_lshlrev_b32_e32 v116, 16, v147
	v_and_b32_e32 v117, 0xffff0000, v147
	v_pk_fma_f32 v[116:117], v[22:23], v[24:25], v[116:117]
	v_cvt_pk_bf16_f32 v22, v30, v31
	v_cvt_pk_bf16_f32 v23, v32, v33
	v_cvt_pk_bf16_f32 v24, v114, v115
	v_cvt_pk_bf16_f32 v25, v116, v117
	v_mov_b32_e32 v216, v22
	v_mov_b32_e32 v217, v23
	v_mov_b32_e32 v218, v24
	v_mov_b32_e32 v219, v25
	s_mov_b64 exec, s[34:35]
	global_store_dwordx4 v[122:123], v[22:25], off offset:256
	s_mov_b64 exec, -1
	v_add_u32_e32 v114, 0x80, v162
	v_ashrrev_i32_e32 v115, 31, v114
	v_mov_b64_e32 v[22:23], s[12:13]
	v_mad_i64_i32 v[22:23], s[28:29], v114, s66, v[22:23]
	v_lshl_add_u64 v[22:23], s[26:27], 1, v[22:23]
	v_lshl_add_u64 v[22:23], v[22:23], 0, v[0:1]
	global_load_dwordx4 v[30:33], v[22:23], off
	v_lshlrev_b64 v[24:25], 11, v[114:115]
	v_lshl_add_u64 v[120:121], s[10:11], 0, v[24:25]
	v_mov_b32_e32 v118, 0
	s_and_b64 vcc, exec, s[0:1]
	v_mov_b32_e32 v124, 0
	v_mov_b32_e32 v125, 0
	v_mov_b32_e32 v122, 0
	v_mov_b32_e32 v123, 0
	s_cbranch_vccnz .LBB0_820
	v_lshl_add_u64 v[24:25], v[120:121], 0, v[0:1]
	global_load_dwordx2 v[124:125], v[24:25], off sc1
	global_load_dwordx2 v[122:123], v[24:25], off offset:8 sc1
